# MoE up K loop: the 8 phases merged into 4 (16 MFMAs per barrier interval, half the barriers)
# baseline (speedup 1.0000x reference)
.LBB0_1418:
	s_add_i32 s65, 0, 0x10000
	v_add_u32_e32 v130, s65, v168
	ds_read_b128 v[2:5], v130
	ds_read_b128 v[6:9], v130 offset:1024
	ds_read_b128 v[10:13], v130 offset:2048
	ds_read_b128 v[14:17], v130 offset:3072
	s_add_u32 s62, s18, 0x20080
	s_addc_u32 s63, s19, 0
	s_add_i32 s13, s43, 0xc000
	v_lshl_add_u64 v[50:51], s[62:63], 0, v[152:153]
	s_mov_b32 m0, s13
	s_add_i32 s64, s43, 0xe000
	ds_read_b128 v[18:21], v170
	ds_read_b128 v[22:25], v170 offset:1024
	ds_read_b128 v[26:29], v170 offset:2048
	ds_read_b128 v[30:33], v170 offset:3072
	ds_read_b128 v[34:37], v170 offset:4096
	ds_read_b128 v[38:41], v170 offset:5120
	ds_read_b128 v[42:45], v170 offset:6144
	ds_read_b128 v[46:49], v170 offset:7168
	global_load_lds_dwordx4 v[50:51], off
	v_lshl_add_u64 v[50:51], s[62:63], 0, v[148:149]
	s_mov_b32 m0, s64
	s_nop 0
	global_load_lds_dwordx4 v[50:51], off
	s_waitcnt lgkmcnt(8)
	s_waitcnt vmcnt(10)
	s_barrier
	s_waitcnt lgkmcnt(6)
	v_mfma_scale_f32_16x16x128_f8f6f4 v[140:143], v[2:9], v[18:25], 0, v205, v205 op_sel_hi:[0,0,0]
	v_mfma_scale_f32_16x16x128_f8f6f4 v[132:135], v[10:17], v[18:25], 0, v205, v205 op_sel_hi:[0,0,0]
	s_waitcnt lgkmcnt(4)
	v_mfma_scale_f32_16x16x128_f8f6f4 v[122:125], v[2:9], v[26:33], 0, v205, v205 op_sel_hi:[0,0,0]
	v_mfma_scale_f32_16x16x128_f8f6f4 v[114:117], v[10:17], v[26:33], 0, v205, v205 op_sel_hi:[0,0,0]
	s_waitcnt lgkmcnt(2)
	v_mfma_scale_f32_16x16x128_f8f6f4 v[106:109], v[2:9], v[34:41], 0, v205, v205 op_sel_hi:[0,0,0]
	v_mfma_scale_f32_16x16x128_f8f6f4 v[98:101], v[10:17], v[34:41], 0, v205, v205 op_sel_hi:[0,0,0]
	s_waitcnt lgkmcnt(0)
	v_mfma_scale_f32_16x16x128_f8f6f4 v[90:93], v[2:9], v[42:49], 0, v205, v205 op_sel_hi:[0,0,0]
	v_mfma_scale_f32_16x16x128_f8f6f4 v[78:81], v[10:17], v[42:49], 0, v205, v205 op_sel_hi:[0,0,0]
	s_barrier
	s_add_i32 s67, 0, 0x14000
	v_lshl_add_u64 v[164:165], s[60:61], 0, v[154:155]
	s_mov_b64 s[62:63], 0x100
	s_add_i32 s65, s65, s38
	v_add_u32_e32 v171, s67, v168
	v_lshl_add_u64 v[50:51], v[164:165], 0, s[62:63]
	s_mov_b32 m0, s65
	v_lshl_add_u64 v[166:167], s[60:61], 0, v[150:151]
	s_add_i32 s66, s65, 0x2000
	ds_read_b128 v[178:181], v171
	ds_read_b128 v[182:185], v171 offset:1024
	ds_read_b128 v[186:189], v171 offset:2048
	ds_read_b128 v[190:193], v171 offset:3072
	global_load_lds_dwordx4 v[50:51], off
	v_lshl_add_u64 v[50:51], v[166:167], 0, s[62:63]
	s_mov_b32 m0, s66
	s_nop 0
	global_load_lds_dwordx4 v[50:51], off
	s_waitcnt vmcnt(10)
	s_barrier
	s_waitcnt lgkmcnt(2)
	v_mfma_scale_f32_16x16x128_f8f6f4 v[144:147], v[178:185], v[18:25], 0, v205, v205 op_sel_hi:[0,0,0]
	s_waitcnt lgkmcnt(0)
	v_mfma_scale_f32_16x16x128_f8f6f4 v[136:139], v[186:193], v[18:25], 0, v205, v205 op_sel_hi:[0,0,0]
	v_mfma_scale_f32_16x16x128_f8f6f4 v[126:129], v[178:185], v[26:33], 0, v205, v205 op_sel_hi:[0,0,0]
	v_mfma_scale_f32_16x16x128_f8f6f4 v[118:121], v[186:193], v[26:33], 0, v205, v205 op_sel_hi:[0,0,0]
	v_mfma_scale_f32_16x16x128_f8f6f4 v[110:113], v[178:185], v[34:41], 0, v205, v205 op_sel_hi:[0,0,0]
	v_mfma_scale_f32_16x16x128_f8f6f4 v[102:105], v[186:193], v[34:41], 0, v205, v205 op_sel_hi:[0,0,0]
	v_mfma_scale_f32_16x16x128_f8f6f4 v[94:97], v[178:185], v[42:49], 0, v205, v205 op_sel_hi:[0,0,0]
	v_mfma_scale_f32_16x16x128_f8f6f4 v[86:89], v[186:193], v[42:49], 0, v205, v205 op_sel_hi:[0,0,0]
	v_lshl_add_u64 v[160:161], s[18:19], 0, v[152:153]
	s_mov_b32 m0, s43
	v_lshl_add_u64 v[18:19], v[160:161], 0, s[62:63]
	v_lshl_add_u64 v[162:163], s[18:19], 0, v[148:149]
	s_barrier
	ds_read_b128 v[194:197], v170 offset:16384
	ds_read_b128 v[198:201], v170 offset:17408
	ds_read_b128 v[218:221], v170 offset:18432
	ds_read_b128 v[222:225], v170 offset:19456
	ds_read_b128 v[226:229], v170 offset:20480
	ds_read_b128 v[230:233], v170 offset:21504
	ds_read_b128 v[234:237], v170 offset:22528
	ds_read_b128 v[238:241], v170 offset:23552
	global_load_lds_dwordx4 v[18:19], off
	v_lshl_add_u64 v[18:19], v[162:163], 0, s[62:63]
	s_mov_b32 m0, s44
	s_nop 0
	global_load_lds_dwordx4 v[18:19], off
	s_barrier
	s_waitcnt lgkmcnt(6)
	v_mfma_scale_f32_16x16x128_f8f6f4 v[74:77], v[2:9], v[194:201], 0, v205, v205 op_sel_hi:[0,0,0]
	v_mfma_scale_f32_16x16x128_f8f6f4 v[66:69], v[10:17], v[194:201], 0, v205, v205 op_sel_hi:[0,0,0]
	s_waitcnt lgkmcnt(4)
	v_mfma_scale_f32_16x16x128_f8f6f4 v[58:61], v[2:9], v[218:225], 0, v205, v205 op_sel_hi:[0,0,0]
	v_mfma_scale_f32_16x16x128_f8f6f4 v[50:53], v[10:17], v[218:225], 0, v205, v205 op_sel_hi:[0,0,0]
	s_waitcnt lgkmcnt(2)
	v_mfma_scale_f32_16x16x128_f8f6f4 v[42:45], v[2:9], v[226:233], 0, v205, v205 op_sel_hi:[0,0,0]
	v_mfma_scale_f32_16x16x128_f8f6f4 v[34:37], v[10:17], v[226:233], 0, v205, v205 op_sel_hi:[0,0,0]
	s_waitcnt lgkmcnt(0)
	v_mfma_scale_f32_16x16x128_f8f6f4 v[26:29], v[2:9], v[234:241], 0, v205, v205 op_sel_hi:[0,0,0]
	v_mfma_scale_f32_16x16x128_f8f6f4 v[18:21], v[10:17], v[234:241], 0, v205, v205 op_sel_hi:[0,0,0]
	s_barrier
	s_add_u32 s62, s60, 0x2100
	s_addc_u32 s63, s61, 0
	s_add_i32 s67, s67, s38
	v_lshl_add_u64 v[2:3], s[62:63], 0, v[154:155]
	s_mov_b32 m0, s67
	s_add_i32 s68, s67, 0x2000
	global_load_lds_dwordx4 v[2:3], off
	v_lshl_add_u64 v[2:3], s[62:63], 0, v[150:151]
	s_mov_b32 m0, s68
	s_nop 0
	global_load_lds_dwordx4 v[2:3], off
	s_waitcnt vmcnt(10)
	s_barrier
	v_mfma_scale_f32_16x16x128_f8f6f4 v[82:85], v[178:185], v[194:201], 0, v205, v205 op_sel_hi:[0,0,0]
	v_mfma_scale_f32_16x16x128_f8f6f4 v[70:73], v[186:193], v[194:201], 0, v205, v205 op_sel_hi:[0,0,0]
	v_mfma_scale_f32_16x16x128_f8f6f4 v[62:65], v[178:185], v[218:225], 0, v205, v205 op_sel_hi:[0,0,0]
	v_mfma_scale_f32_16x16x128_f8f6f4 v[54:57], v[186:193], v[218:225], 0, v205, v205 op_sel_hi:[0,0,0]
	v_mfma_scale_f32_16x16x128_f8f6f4 v[46:49], v[178:185], v[226:233], 0, v205, v205 op_sel_hi:[0,0,0]
	v_mfma_scale_f32_16x16x128_f8f6f4 v[38:41], v[186:193], v[226:233], 0, v205, v205 op_sel_hi:[0,0,0]
	v_mfma_scale_f32_16x16x128_f8f6f4 v[30:33], v[178:185], v[234:241], 0, v205, v205 op_sel_hi:[0,0,0]
	v_mfma_scale_f32_16x16x128_f8f6f4 v[22:25], v[186:193], v[234:241], 0, v205, v205 op_sel_hi:[0,0,0]
	s_add_i32 s69, 0, 0x18000
	v_add_u32_e32 v172, s69, v168
	s_barrier
	ds_read_b128 v[10:13], v172
	ds_read_b128 v[14:17], v172 offset:1024
	ds_read_b128 v[2:5], v172 offset:2048
	ds_read_b128 v[6:9], v172 offset:3072
	s_add_u32 s62, s18, 0x20100
	s_addc_u32 s63, s19, 0
	s_mov_b32 m0, s45
	v_lshl_add_u64 v[174:175], s[62:63], 0, v[152:153]
	ds_read_b128 v[178:181], v170 offset:32768
	ds_read_b128 v[182:185], v170 offset:33792
	ds_read_b128 v[186:189], v170 offset:34816
	ds_read_b128 v[190:193], v170 offset:35840
	ds_read_b128 v[194:197], v170 offset:36864
	ds_read_b128 v[198:201], v170 offset:37888
	ds_read_b128 v[218:221], v170 offset:38912
	ds_read_b128 v[222:225], v170 offset:39936
	global_load_lds_dwordx4 v[174:175], off
	v_lshl_add_u64 v[174:175], s[62:63], 0, v[148:149]
	s_mov_b32 m0, s46
	s_nop 0
	global_load_lds_dwordx4 v[174:175], off
	s_waitcnt lgkmcnt(8)
	s_waitcnt vmcnt(10)
	s_barrier
	s_waitcnt lgkmcnt(6)
	v_mfma_scale_f32_16x16x128_f8f6f4 v[140:143], v[10:17], v[178:185], v[140:143], v205, v205 op_sel_hi:[0,0,0]
	v_mfma_scale_f32_16x16x128_f8f6f4 v[132:135], v[2:9], v[178:185], v[132:135], v205, v205 op_sel_hi:[0,0,0]
	s_waitcnt lgkmcnt(4)
	v_mfma_scale_f32_16x16x128_f8f6f4 v[122:125], v[10:17], v[186:193], v[122:125], v205, v205 op_sel_hi:[0,0,0]
	v_mfma_scale_f32_16x16x128_f8f6f4 v[114:117], v[2:9], v[186:193], v[114:117], v205, v205 op_sel_hi:[0,0,0]
	s_waitcnt lgkmcnt(2)
	v_mfma_scale_f32_16x16x128_f8f6f4 v[106:109], v[10:17], v[194:201], v[106:109], v205, v205 op_sel_hi:[0,0,0]
	v_mfma_scale_f32_16x16x128_f8f6f4 v[98:101], v[2:9], v[194:201], v[98:101], v205, v205 op_sel_hi:[0,0,0]
	s_waitcnt lgkmcnt(0)
	v_mfma_scale_f32_16x16x128_f8f6f4 v[90:93], v[10:17], v[218:225], v[90:93], v205, v205 op_sel_hi:[0,0,0]
	v_mfma_scale_f32_16x16x128_f8f6f4 v[78:81], v[2:9], v[218:225], v[78:81], v205, v205 op_sel_hi:[0,0,0]
	s_barrier
	s_add_i32 s71, 0, 0x1c000
	s_mov_b64 s[62:63], 0x180
	s_add_i32 s69, s69, s38
	v_add_u32_e32 v173, s71, v168
	v_lshl_add_u64 v[164:165], v[164:165], 0, s[62:63]
	s_mov_b32 m0, s69
	s_add_i32 s70, s69, 0x2000
	ds_read_b128 v[226:229], v173
	ds_read_b128 v[230:233], v173 offset:1024
	ds_read_b128 v[234:237], v173 offset:2048
	ds_read_b128 v[238:241], v173 offset:3072
	global_load_lds_dwordx4 v[164:165], off
	v_lshl_add_u64 v[164:165], v[166:167], 0, s[62:63]
	s_mov_b32 m0, s70
	s_nop 0
	global_load_lds_dwordx4 v[164:165], off
	s_waitcnt vmcnt(10)
	s_barrier
	s_waitcnt lgkmcnt(2)
	v_mfma_scale_f32_16x16x128_f8f6f4 v[144:147], v[226:233], v[178:185], v[144:147], v205, v205 op_sel_hi:[0,0,0]
	s_waitcnt lgkmcnt(0)
	v_mfma_scale_f32_16x16x128_f8f6f4 v[136:139], v[234:241], v[178:185], v[136:139], v205, v205 op_sel_hi:[0,0,0]
	v_mfma_scale_f32_16x16x128_f8f6f4 v[126:129], v[226:233], v[186:193], v[126:129], v205, v205 op_sel_hi:[0,0,0]
	v_mfma_scale_f32_16x16x128_f8f6f4 v[118:121], v[234:241], v[186:193], v[118:121], v205, v205 op_sel_hi:[0,0,0]
	v_mfma_scale_f32_16x16x128_f8f6f4 v[110:113], v[226:233], v[194:201], v[110:113], v205, v205 op_sel_hi:[0,0,0]
	v_mfma_scale_f32_16x16x128_f8f6f4 v[102:105], v[234:241], v[194:201], v[102:105], v205, v205 op_sel_hi:[0,0,0]
	v_mfma_scale_f32_16x16x128_f8f6f4 v[94:97], v[226:233], v[218:225], v[94:97], v205, v205 op_sel_hi:[0,0,0]
	v_mfma_scale_f32_16x16x128_f8f6f4 v[86:89], v[234:241], v[218:225], v[86:89], v205, v205 op_sel_hi:[0,0,0]
	s_mov_b32 m0, s51
	v_lshl_add_u64 v[160:161], v[160:161], 0, s[62:63]
	s_barrier
	ds_read_b128 v[178:181], v170 offset:49152
	ds_read_b128 v[182:185], v170 offset:50176
	ds_read_b128 v[186:189], v170 offset:51200
	ds_read_b128 v[190:193], v170 offset:52224
	ds_read_b128 v[194:197], v170 offset:53248
	ds_read_b128 v[198:201], v170 offset:54272
	ds_read_b128 v[218:221], v170 offset:55296
	ds_read_b128 v[222:225], v170 offset:56320
	global_load_lds_dwordx4 v[160:161], off
	v_lshl_add_u64 v[160:161], v[162:163], 0, s[62:63]
	s_mov_b32 m0, s53
	s_nop 0
	global_load_lds_dwordx4 v[160:161], off
	s_barrier
	s_waitcnt lgkmcnt(6)
	v_mfma_scale_f32_16x16x128_f8f6f4 v[74:77], v[10:17], v[178:185], v[74:77], v205, v205 op_sel_hi:[0,0,0]
	v_mfma_scale_f32_16x16x128_f8f6f4 v[66:69], v[2:9], v[178:185], v[66:69], v205, v205 op_sel_hi:[0,0,0]
	s_waitcnt lgkmcnt(4)
	v_mfma_scale_f32_16x16x128_f8f6f4 v[58:61], v[10:17], v[186:193], v[58:61], v205, v205 op_sel_hi:[0,0,0]
	v_mfma_scale_f32_16x16x128_f8f6f4 v[50:53], v[2:9], v[186:193], v[50:53], v205, v205 op_sel_hi:[0,0,0]
	s_waitcnt lgkmcnt(2)
	v_mfma_scale_f32_16x16x128_f8f6f4 v[42:45], v[10:17], v[194:201], v[42:45], v205, v205 op_sel_hi:[0,0,0]
	v_mfma_scale_f32_16x16x128_f8f6f4 v[34:37], v[2:9], v[194:201], v[34:37], v205, v205 op_sel_hi:[0,0,0]
	s_waitcnt lgkmcnt(0)
	v_mfma_scale_f32_16x16x128_f8f6f4 v[26:29], v[10:17], v[218:225], v[26:29], v205, v205 op_sel_hi:[0,0,0]
	v_mfma_scale_f32_16x16x128_f8f6f4 v[18:21], v[2:9], v[218:225], v[18:21], v205, v205 op_sel_hi:[0,0,0]
	s_barrier
	s_add_u32 s62, s60, 0x2180
	s_addc_u32 s63, s61, 0
	s_add_i32 s71, s71, s38
	v_lshl_add_u64 v[2:3], s[62:63], 0, v[154:155]
	s_mov_b32 m0, s71
	s_add_i32 s72, s71, 0x2000
	global_load_lds_dwordx4 v[2:3], off
	v_lshl_add_u64 v[2:3], s[62:63], 0, v[150:151]
	s_mov_b32 m0, s72
	s_nop 0
	global_load_lds_dwordx4 v[2:3], off
	s_waitcnt vmcnt(8)
	s_barrier
	v_mfma_scale_f32_16x16x128_f8f6f4 v[82:85], v[226:233], v[178:185], v[82:85], v205, v205 op_sel_hi:[0,0,0]
	v_mfma_scale_f32_16x16x128_f8f6f4 v[70:73], v[234:241], v[178:185], v[70:73], v205, v205 op_sel_hi:[0,0,0]
	v_mfma_scale_f32_16x16x128_f8f6f4 v[62:65], v[226:233], v[186:193], v[62:65], v205, v205 op_sel_hi:[0,0,0]
	v_mfma_scale_f32_16x16x128_f8f6f4 v[54:57], v[234:241], v[186:193], v[54:57], v205, v205 op_sel_hi:[0,0,0]
	v_mfma_scale_f32_16x16x128_f8f6f4 v[46:49], v[226:233], v[194:201], v[46:49], v205, v205 op_sel_hi:[0,0,0]
	v_mfma_scale_f32_16x16x128_f8f6f4 v[38:41], v[234:241], v[194:201], v[38:41], v205, v205 op_sel_hi:[0,0,0]
	v_mfma_scale_f32_16x16x128_f8f6f4 v[30:33], v[226:233], v[218:225], v[30:33], v205, v205 op_sel_hi:[0,0,0]
	v_mfma_scale_f32_16x16x128_f8f6f4 v[22:25], v[234:241], v[218:225], v[22:25], v205, v205 op_sel_hi:[0,0,0]
	s_add_u32 s18, s18, 0x20180
	s_addc_u32 s19, s19, 0
	s_add_u32 s73, s60, 0x200
	s_addc_u32 s74, s61, 0
	s_mov_b32 s75, 0
	s_barrier
.LBB0_1419:
	ds_read_b128 v[10:13], v130
	ds_read_b128 v[14:17], v130 offset:1024
	ds_read_b128 v[160:163], v130 offset:2048
	ds_read_b128 v[164:167], v130 offset:3072
	s_add_u32 s60, s18, 0xfffe0080
	s_addc_u32 s61, s19, -1
	s_cmp_eq_u32 s75, 4
	s_cselect_b32 s63, s15, s61
	s_cselect_b32 s62, s14, s60
	s_cselect_b32 s61, s17, s74
	s_cselect_b32 s60, s16, s73
	s_mov_b32 m0, s13
	v_lshl_add_u64 v[2:3], s[18:19], 0, v[156:157]
	ds_read_b128 v[178:181], v170
	ds_read_b128 v[182:185], v170 offset:1024
	ds_read_b128 v[186:189], v170 offset:2048
	ds_read_b128 v[190:193], v170 offset:3072
	ds_read_b128 v[194:197], v170 offset:4096
	ds_read_b128 v[198:201], v170 offset:5120
	ds_read_b128 v[218:221], v170 offset:6144
	ds_read_b128 v[222:225], v170 offset:7168
	global_load_lds_dwordx4 v[2:3], off
	v_lshl_add_u64 v[2:3], s[18:19], 0, v[158:159]
	s_mov_b32 m0, s64
	s_nop 0
	global_load_lds_dwordx4 v[2:3], off
	ds_read_b128 v[226:229], v171
	ds_read_b128 v[230:233], v171 offset:1024
	ds_read_b128 v[234:237], v171 offset:2048
	ds_read_b128 v[238:241], v171 offset:3072
	s_waitcnt vmcnt(8)
	s_barrier
	s_waitcnt lgkmcnt(10)
	v_mfma_scale_f32_16x16x128_f8f6f4 v[140:143], v[10:17], v[178:185], v[140:143], v205, v205 op_sel_hi:[0,0,0]
	v_mfma_scale_f32_16x16x128_f8f6f4 v[132:135], v[160:167], v[178:185], v[132:135], v205, v205 op_sel_hi:[0,0,0]
	s_waitcnt lgkmcnt(8)
	v_mfma_scale_f32_16x16x128_f8f6f4 v[122:125], v[10:17], v[186:193], v[122:125], v205, v205 op_sel_hi:[0,0,0]
	v_mfma_scale_f32_16x16x128_f8f6f4 v[114:117], v[160:167], v[186:193], v[114:117], v205, v205 op_sel_hi:[0,0,0]
	s_waitcnt lgkmcnt(6)
	v_mfma_scale_f32_16x16x128_f8f6f4 v[106:109], v[10:17], v[194:201], v[106:109], v205, v205 op_sel_hi:[0,0,0]
	v_mfma_scale_f32_16x16x128_f8f6f4 v[98:101], v[160:167], v[194:201], v[98:101], v205, v205 op_sel_hi:[0,0,0]
	s_waitcnt lgkmcnt(4)
	v_mfma_scale_f32_16x16x128_f8f6f4 v[90:93], v[10:17], v[218:225], v[90:93], v205, v205 op_sel_hi:[0,0,0]
	v_mfma_scale_f32_16x16x128_f8f6f4 v[78:81], v[160:167], v[218:225], v[78:81], v205, v205 op_sel_hi:[0,0,0]
	s_waitcnt lgkmcnt(2)
	v_mfma_scale_f32_16x16x128_f8f6f4 v[144:147], v[226:233], v[178:185], v[144:147], v205, v205 op_sel_hi:[0,0,0]
	s_waitcnt lgkmcnt(0)
	v_mfma_scale_f32_16x16x128_f8f6f4 v[136:139], v[234:241], v[178:185], v[136:139], v205, v205 op_sel_hi:[0,0,0]
	v_mfma_scale_f32_16x16x128_f8f6f4 v[126:129], v[226:233], v[186:193], v[126:129], v205, v205 op_sel_hi:[0,0,0]
	v_mfma_scale_f32_16x16x128_f8f6f4 v[118:121], v[234:241], v[186:193], v[118:121], v205, v205 op_sel_hi:[0,0,0]
	v_mfma_scale_f32_16x16x128_f8f6f4 v[110:113], v[226:233], v[194:201], v[110:113], v205, v205 op_sel_hi:[0,0,0]
	v_mfma_scale_f32_16x16x128_f8f6f4 v[102:105], v[234:241], v[194:201], v[102:105], v205, v205 op_sel_hi:[0,0,0]
	v_mfma_scale_f32_16x16x128_f8f6f4 v[94:97], v[226:233], v[218:225], v[94:97], v205, v205 op_sel_hi:[0,0,0]
	v_mfma_scale_f32_16x16x128_f8f6f4 v[86:89], v[234:241], v[218:225], v[86:89], v205, v205 op_sel_hi:[0,0,0]
	s_barrier
	s_mov_b32 m0, s65
	v_lshl_add_u64 v[6:7], s[60:61], 0, v[154:155]
	global_load_lds_dwordx4 v[6:7], off
	v_lshl_add_u64 v[8:9], s[60:61], 0, v[150:151]
	s_mov_b32 m0, s66
	s_nop 0
	global_load_lds_dwordx4 v[8:9], off
	s_mov_b32 m0, s43
	v_lshl_add_u64 v[2:3], s[62:63], 0, v[152:153]
	ds_read_b128 v[178:181], v170 offset:16384
	ds_read_b128 v[182:185], v170 offset:17408
	ds_read_b128 v[186:189], v170 offset:18432
	ds_read_b128 v[190:193], v170 offset:19456
	ds_read_b128 v[194:197], v170 offset:20480
	ds_read_b128 v[198:201], v170 offset:21504
	ds_read_b128 v[218:221], v170 offset:22528
	ds_read_b128 v[222:225], v170 offset:23552
	global_load_lds_dwordx4 v[2:3], off
	v_lshl_add_u64 v[4:5], s[62:63], 0, v[148:149]
	s_mov_b32 m0, s44
	s_nop 0
	global_load_lds_dwordx4 v[4:5], off
	s_add_u32 s76, s60, 0x2000
	s_addc_u32 s77, s61, 0
	s_mov_b32 m0, s67
	v_lshl_add_u64 v[242:243], s[76:77], 0, v[154:155]
	global_load_lds_dwordx4 v[242:243], off
	v_lshl_add_u64 v[242:243], s[76:77], 0, v[150:151]
	s_mov_b32 m0, s68
	s_nop 0
	global_load_lds_dwordx4 v[242:243], off
	s_waitcnt vmcnt(8)
	s_barrier
	s_waitcnt lgkmcnt(6)
	v_mfma_scale_f32_16x16x128_f8f6f4 v[74:77], v[10:17], v[178:185], v[74:77], v205, v205 op_sel_hi:[0,0,0]
	v_mfma_scale_f32_16x16x128_f8f6f4 v[66:69], v[160:167], v[178:185], v[66:69], v205, v205 op_sel_hi:[0,0,0]
	s_waitcnt lgkmcnt(4)
	v_mfma_scale_f32_16x16x128_f8f6f4 v[58:61], v[10:17], v[186:193], v[58:61], v205, v205 op_sel_hi:[0,0,0]
	v_mfma_scale_f32_16x16x128_f8f6f4 v[50:53], v[160:167], v[186:193], v[50:53], v205, v205 op_sel_hi:[0,0,0]
	s_waitcnt lgkmcnt(2)
	v_mfma_scale_f32_16x16x128_f8f6f4 v[42:45], v[10:17], v[194:201], v[42:45], v205, v205 op_sel_hi:[0,0,0]
	v_mfma_scale_f32_16x16x128_f8f6f4 v[34:37], v[160:167], v[194:201], v[34:37], v205, v205 op_sel_hi:[0,0,0]
	s_waitcnt lgkmcnt(0)
	v_mfma_scale_f32_16x16x128_f8f6f4 v[26:29], v[10:17], v[218:225], v[26:29], v205, v205 op_sel_hi:[0,0,0]
	v_mfma_scale_f32_16x16x128_f8f6f4 v[18:21], v[160:167], v[218:225], v[18:21], v205, v205 op_sel_hi:[0,0,0]
	v_mfma_scale_f32_16x16x128_f8f6f4 v[82:85], v[226:233], v[178:185], v[82:85], v205, v205 op_sel_hi:[0,0,0]
	v_mfma_scale_f32_16x16x128_f8f6f4 v[70:73], v[234:241], v[178:185], v[70:73], v205, v205 op_sel_hi:[0,0,0]
	v_mfma_scale_f32_16x16x128_f8f6f4 v[62:65], v[226:233], v[186:193], v[62:65], v205, v205 op_sel_hi:[0,0,0]
	v_mfma_scale_f32_16x16x128_f8f6f4 v[54:57], v[234:241], v[186:193], v[54:57], v205, v205 op_sel_hi:[0,0,0]
	v_mfma_scale_f32_16x16x128_f8f6f4 v[46:49], v[226:233], v[194:201], v[46:49], v205, v205 op_sel_hi:[0,0,0]
	v_mfma_scale_f32_16x16x128_f8f6f4 v[38:41], v[234:241], v[194:201], v[38:41], v205, v205 op_sel_hi:[0,0,0]
	v_mfma_scale_f32_16x16x128_f8f6f4 v[30:33], v[226:233], v[218:225], v[30:33], v205, v205 op_sel_hi:[0,0,0]
	v_mfma_scale_f32_16x16x128_f8f6f4 v[22:25], v[234:241], v[218:225], v[22:25], v205, v205 op_sel_hi:[0,0,0]
	s_barrier
	ds_read_b128 v[10:13], v172
	ds_read_b128 v[14:17], v172 offset:1024
	ds_read_b128 v[160:163], v172 offset:2048
	ds_read_b128 v[164:167], v172 offset:3072
	s_add_u32 s62, s62, 0x20000
	s_addc_u32 s63, s63, 0
	s_mov_b32 m0, s45
	v_lshl_add_u64 v[174:175], s[62:63], 0, v[152:153]
	ds_read_b128 v[178:181], v170 offset:32768
	ds_read_b128 v[182:185], v170 offset:33792
	ds_read_b128 v[186:189], v170 offset:34816
	ds_read_b128 v[190:193], v170 offset:35840
	ds_read_b128 v[194:197], v170 offset:36864
	ds_read_b128 v[198:201], v170 offset:37888
	ds_read_b128 v[218:221], v170 offset:38912
	ds_read_b128 v[222:225], v170 offset:39936
	global_load_lds_dwordx4 v[174:175], off
	v_lshl_add_u64 v[174:175], s[62:63], 0, v[148:149]
	s_mov_b32 m0, s46
	s_nop 0
	global_load_lds_dwordx4 v[174:175], off
	ds_read_b128 v[226:229], v173
	ds_read_b128 v[230:233], v173 offset:1024
	ds_read_b128 v[234:237], v173 offset:2048
	ds_read_b128 v[238:241], v173 offset:3072
	s_waitcnt vmcnt(8)
	s_barrier
	s_waitcnt lgkmcnt(10)
	v_mfma_scale_f32_16x16x128_f8f6f4 v[140:143], v[10:17], v[178:185], v[140:143], v205, v205 op_sel_hi:[0,0,0]
	v_mfma_scale_f32_16x16x128_f8f6f4 v[132:135], v[160:167], v[178:185], v[132:135], v205, v205 op_sel_hi:[0,0,0]
	s_waitcnt lgkmcnt(8)
	v_mfma_scale_f32_16x16x128_f8f6f4 v[122:125], v[10:17], v[186:193], v[122:125], v205, v205 op_sel_hi:[0,0,0]
	v_mfma_scale_f32_16x16x128_f8f6f4 v[114:117], v[160:167], v[186:193], v[114:117], v205, v205 op_sel_hi:[0,0,0]
	s_waitcnt lgkmcnt(6)
	v_mfma_scale_f32_16x16x128_f8f6f4 v[106:109], v[10:17], v[194:201], v[106:109], v205, v205 op_sel_hi:[0,0,0]
	v_mfma_scale_f32_16x16x128_f8f6f4 v[98:101], v[160:167], v[194:201], v[98:101], v205, v205 op_sel_hi:[0,0,0]
	s_waitcnt lgkmcnt(4)
	v_mfma_scale_f32_16x16x128_f8f6f4 v[90:93], v[10:17], v[218:225], v[90:93], v205, v205 op_sel_hi:[0,0,0]
	v_mfma_scale_f32_16x16x128_f8f6f4 v[78:81], v[160:167], v[218:225], v[78:81], v205, v205 op_sel_hi:[0,0,0]
	s_waitcnt lgkmcnt(2)
	v_mfma_scale_f32_16x16x128_f8f6f4 v[144:147], v[226:233], v[178:185], v[144:147], v205, v205 op_sel_hi:[0,0,0]
	s_waitcnt lgkmcnt(0)
	v_mfma_scale_f32_16x16x128_f8f6f4 v[136:139], v[234:241], v[178:185], v[136:139], v205, v205 op_sel_hi:[0,0,0]
	v_mfma_scale_f32_16x16x128_f8f6f4 v[126:129], v[226:233], v[186:193], v[126:129], v205, v205 op_sel_hi:[0,0,0]
	v_mfma_scale_f32_16x16x128_f8f6f4 v[118:121], v[234:241], v[186:193], v[118:121], v205, v205 op_sel_hi:[0,0,0]
	v_mfma_scale_f32_16x16x128_f8f6f4 v[110:113], v[226:233], v[194:201], v[110:113], v205, v205 op_sel_hi:[0,0,0]
	v_mfma_scale_f32_16x16x128_f8f6f4 v[102:105], v[234:241], v[194:201], v[102:105], v205, v205 op_sel_hi:[0,0,0]
	v_mfma_scale_f32_16x16x128_f8f6f4 v[94:97], v[226:233], v[218:225], v[94:97], v205, v205 op_sel_hi:[0,0,0]
	v_mfma_scale_f32_16x16x128_f8f6f4 v[86:89], v[234:241], v[218:225], v[86:89], v205, v205 op_sel_hi:[0,0,0]
	s_barrier
	s_mov_b32 m0, s69
	v_lshl_add_u64 v[6:7], v[6:7], 0, s[30:31]
	global_load_lds_dwordx4 v[6:7], off
	v_lshl_add_u64 v[6:7], v[8:9], 0, s[30:31]
	s_mov_b32 m0, s70
	s_nop 0
	global_load_lds_dwordx4 v[6:7], off
	s_mov_b32 m0, s51
	v_lshl_add_u64 v[2:3], v[2:3], 0, s[30:31]
	ds_read_b128 v[178:181], v170 offset:49152
	ds_read_b128 v[182:185], v170 offset:50176
	ds_read_b128 v[186:189], v170 offset:51200
	ds_read_b128 v[190:193], v170 offset:52224
	ds_read_b128 v[194:197], v170 offset:53248
	ds_read_b128 v[198:201], v170 offset:54272
	ds_read_b128 v[218:221], v170 offset:55296
	ds_read_b128 v[222:225], v170 offset:56320
	global_load_lds_dwordx4 v[2:3], off
	v_lshl_add_u64 v[2:3], v[4:5], 0, s[30:31]
	s_mov_b32 m0, s53
	s_nop 0
	global_load_lds_dwordx4 v[2:3], off
	s_add_u32 s60, s60, 0x2080
	s_addc_u32 s61, s61, 0
	s_mov_b32 m0, s71
	v_lshl_add_u64 v[2:3], s[60:61], 0, v[154:155]
	global_load_lds_dwordx4 v[2:3], off
	v_lshl_add_u64 v[2:3], s[60:61], 0, v[150:151]
	s_mov_b32 m0, s72
	s_nop 0
	global_load_lds_dwordx4 v[2:3], off
	s_waitcnt vmcnt(8)
	s_barrier
	s_waitcnt lgkmcnt(6)
	v_mfma_scale_f32_16x16x128_f8f6f4 v[74:77], v[10:17], v[178:185], v[74:77], v205, v205 op_sel_hi:[0,0,0]
	v_mfma_scale_f32_16x16x128_f8f6f4 v[66:69], v[160:167], v[178:185], v[66:69], v205, v205 op_sel_hi:[0,0,0]
	s_waitcnt lgkmcnt(4)
	v_mfma_scale_f32_16x16x128_f8f6f4 v[58:61], v[10:17], v[186:193], v[58:61], v205, v205 op_sel_hi:[0,0,0]
	v_mfma_scale_f32_16x16x128_f8f6f4 v[50:53], v[160:167], v[186:193], v[50:53], v205, v205 op_sel_hi:[0,0,0]
	s_waitcnt lgkmcnt(2)
	v_mfma_scale_f32_16x16x128_f8f6f4 v[42:45], v[10:17], v[194:201], v[42:45], v205, v205 op_sel_hi:[0,0,0]
	v_mfma_scale_f32_16x16x128_f8f6f4 v[34:37], v[160:167], v[194:201], v[34:37], v205, v205 op_sel_hi:[0,0,0]
	s_waitcnt lgkmcnt(0)
	v_mfma_scale_f32_16x16x128_f8f6f4 v[26:29], v[10:17], v[218:225], v[26:29], v205, v205 op_sel_hi:[0,0,0]
	v_mfma_scale_f32_16x16x128_f8f6f4 v[18:21], v[160:167], v[218:225], v[18:21], v205, v205 op_sel_hi:[0,0,0]
	v_mfma_scale_f32_16x16x128_f8f6f4 v[82:85], v[226:233], v[178:185], v[82:85], v205, v205 op_sel_hi:[0,0,0]
	v_mfma_scale_f32_16x16x128_f8f6f4 v[70:73], v[234:241], v[178:185], v[70:73], v205, v205 op_sel_hi:[0,0,0]
	v_mfma_scale_f32_16x16x128_f8f6f4 v[62:65], v[226:233], v[186:193], v[62:65], v205, v205 op_sel_hi:[0,0,0]
	v_mfma_scale_f32_16x16x128_f8f6f4 v[54:57], v[234:241], v[186:193], v[54:57], v205, v205 op_sel_hi:[0,0,0]
	v_mfma_scale_f32_16x16x128_f8f6f4 v[46:49], v[226:233], v[194:201], v[46:49], v205, v205 op_sel_hi:[0,0,0]
	v_mfma_scale_f32_16x16x128_f8f6f4 v[38:41], v[234:241], v[194:201], v[38:41], v205, v205 op_sel_hi:[0,0,0]
	v_mfma_scale_f32_16x16x128_f8f6f4 v[30:33], v[226:233], v[218:225], v[30:33], v205, v205 op_sel_hi:[0,0,0]
	v_mfma_scale_f32_16x16x128_f8f6f4 v[22:25], v[234:241], v[218:225], v[22:25], v205, v205 op_sel_hi:[0,0,0]
	s_add_i32 s75, s75, 2
	s_add_u32 s18, s18, 0x100
	s_addc_u32 s19, s19, 0
	s_add_u32 s73, s73, 0x100
	s_addc_u32 s74, s74, 0
	s_cmp_gt_u32 s75, 5
	s_barrier
	s_cbranch_scc0 .LBB0_1419
	v_mov_b32_e32 v234, 0xbcb8aa3b
	v_mov_b32_e32 v235, 0xbcb8aa3b
	v_mov_b32_e32 v236, 1.0
	v_mov_b32_e32 v237, 1.0
	v_mov_b32_e32 v238, 0x3b000000
	v_mov_b32_e32 v239, 0x3b000000
	v_pk_mul_f32 v[218:219], v[140:141], v[234:235]
	v_pk_mul_f32 v[220:221], v[142:143], v[234:235]
	v_pk_mul_f32 v[226:227], v[132:133], v[234:235]
	v_pk_mul_f32 v[228:229], v[134:135], v[234:235]
	v_exp_f32_e32 v218, v218
	v_exp_f32_e32 v219, v219
	v_exp_f32_e32 v220, v220
	v_exp_f32_e32 v221, v221
	v_exp_f32_e32 v226, v226
	v_exp_f32_e32 v227, v227
	v_exp_f32_e32 v228, v228
	v_exp_f32_e32 v229, v229
	v_pk_mul_f32 v[222:223], v[140:141], v[144:145]
	v_pk_mul_f32 v[224:225], v[142:143], v[146:147]
	v_pk_mul_f32 v[230:231], v[132:133], v[136:137]
	v_pk_mul_f32 v[232:233], v[134:135], v[138:139]
	v_pk_add_f32 v[218:219], v[236:237], v[218:219]
	v_pk_add_f32 v[220:221], v[236:237], v[220:221]
	v_pk_add_f32 v[226:227], v[236:237], v[226:227]
	v_pk_add_f32 v[228:229], v[236:237], v[228:229]
	v_rcp_f32_e32 v218, v218
	v_rcp_f32_e32 v219, v219
	v_rcp_f32_e32 v220, v220
	v_rcp_f32_e32 v221, v221
	v_rcp_f32_e32 v226, v226
	v_rcp_f32_e32 v227, v227
	v_rcp_f32_e32 v228, v228
	v_rcp_f32_e32 v229, v229
	v_pk_mul_f32 v[222:223], v[238:239], v[222:223]
	v_pk_mul_f32 v[224:225], v[238:239], v[224:225]
	v_pk_mul_f32 v[230:231], v[238:239], v[230:231]
	v_pk_mul_f32 v[232:233], v[238:239], v[232:233]
	v_pk_mul_f32 v[222:223], v[218:219], v[222:223]
	v_pk_mul_f32 v[224:225], v[220:221], v[224:225]
	v_pk_mul_f32 v[230:231], v[226:227], v[230:231]
	v_pk_mul_f32 v[232:233], v[228:229], v[232:233]
	v_med3_f32 v222, v222, s26, v209
	v_med3_f32 v223, v223, s26, v209
	v_med3_f32 v224, v224, s26, v209
	v_med3_f32 v225, v225, s26, v209
	v_med3_f32 v230, v230, s26, v209
	v_med3_f32 v231, v231, s26, v209
	v_med3_f32 v232, v232, s26, v209
	v_med3_f32 v233, v233, s26, v209
	v_cvt_pk_fp8_f32 v4, v222, v223
	v_cvt_pk_fp8_f32 v4, v224, v225 op_sel:[0,0,1]
	v_cvt_pk_fp8_f32 v5, v230, v231
	v_cvt_pk_fp8_f32 v5, v232, v233 op_sel:[0,0,1]
	s_ashr_i32 s13, s12, 31
	s_lshl_b64 s[12:13], s[12:13], 11
	s_add_u32 s12, s47, s12
	s_addc_u32 s13, s50, s13
	s_ashr_i32 s14, s59, 31
	s_add_u32 s12, s12, s59
	s_addc_u32 s13, s13, s14
	v_mov_b32_e32 v130, v169
	s_nop 15
	s_nop 15
	global_store_dwordx2 v130, v[4:5], s[12:13]
	v_pk_mul_f32 v[218:219], v[122:123], v[234:235]
	v_pk_mul_f32 v[220:221], v[124:125], v[234:235]
	v_pk_mul_f32 v[226:227], v[114:115], v[234:235]
	v_pk_mul_f32 v[228:229], v[116:117], v[234:235]
	v_exp_f32_e32 v218, v218
	v_exp_f32_e32 v219, v219
	v_exp_f32_e32 v220, v220
	v_exp_f32_e32 v221, v221
	v_exp_f32_e32 v226, v226
	v_exp_f32_e32 v227, v227
	v_exp_f32_e32 v228, v228
	v_exp_f32_e32 v229, v229
	v_pk_mul_f32 v[222:223], v[122:123], v[126:127]
	v_pk_mul_f32 v[224:225], v[124:125], v[128:129]
	v_pk_mul_f32 v[230:231], v[114:115], v[118:119]
	v_pk_mul_f32 v[232:233], v[116:117], v[120:121]
	v_pk_add_f32 v[218:219], v[236:237], v[218:219]
	v_pk_add_f32 v[220:221], v[236:237], v[220:221]
	v_pk_add_f32 v[226:227], v[236:237], v[226:227]
	v_pk_add_f32 v[228:229], v[236:237], v[228:229]
	v_rcp_f32_e32 v218, v218
	v_rcp_f32_e32 v219, v219
	v_rcp_f32_e32 v220, v220
	v_rcp_f32_e32 v221, v221
	v_rcp_f32_e32 v226, v226
	v_rcp_f32_e32 v227, v227
	v_rcp_f32_e32 v228, v228
	v_rcp_f32_e32 v229, v229
	v_pk_mul_f32 v[222:223], v[238:239], v[222:223]
	v_pk_mul_f32 v[224:225], v[238:239], v[224:225]
	v_pk_mul_f32 v[230:231], v[238:239], v[230:231]
	v_pk_mul_f32 v[232:233], v[238:239], v[232:233]
	v_pk_mul_f32 v[222:223], v[218:219], v[222:223]
	v_pk_mul_f32 v[224:225], v[220:221], v[224:225]
	v_pk_mul_f32 v[230:231], v[226:227], v[230:231]
	v_pk_mul_f32 v[232:233], v[228:229], v[232:233]
	v_med3_f32 v222, v222, s26, v209
	v_med3_f32 v223, v223, s26, v209
	v_med3_f32 v224, v224, s26, v209
	v_med3_f32 v225, v225, s26, v209
	v_med3_f32 v230, v230, s26, v209
	v_med3_f32 v231, v231, s26, v209
	v_med3_f32 v232, v232, s26, v209
	v_med3_f32 v233, v233, s26, v209
	v_cvt_pk_fp8_f32 v4, v222, v223
	v_cvt_pk_fp8_f32 v4, v224, v225 op_sel:[0,0,1]
	v_cvt_pk_fp8_f32 v5, v230, v231
	v_cvt_pk_fp8_f32 v5, v232, v233 op_sel:[0,0,1]
	v_lshl_add_u64 v[2:3], s[12:13], 0, v[130:131]
	s_mov_b32 s12, 0x8000
	v_add_co_u32_e32 v6, vcc, s12, v2
	s_nop 0
	v_addc_co_u32_e32 v7, vcc, 0, v3, vcc
	global_store_dwordx2 v[6:7], v[4:5], off
	v_pk_mul_f32 v[218:219], v[106:107], v[234:235]
	v_pk_mul_f32 v[220:221], v[108:109], v[234:235]
	v_pk_mul_f32 v[226:227], v[98:99], v[234:235]
	v_pk_mul_f32 v[228:229], v[100:101], v[234:235]
	v_exp_f32_e32 v218, v218
	v_exp_f32_e32 v219, v219
	v_exp_f32_e32 v220, v220
	v_exp_f32_e32 v221, v221
	v_exp_f32_e32 v226, v226
	v_exp_f32_e32 v227, v227
	v_exp_f32_e32 v228, v228
	v_exp_f32_e32 v229, v229
	v_pk_mul_f32 v[222:223], v[106:107], v[110:111]
	v_pk_mul_f32 v[224:225], v[108:109], v[112:113]
	v_pk_mul_f32 v[230:231], v[98:99], v[102:103]
	v_pk_mul_f32 v[232:233], v[100:101], v[104:105]
	v_pk_add_f32 v[218:219], v[236:237], v[218:219]
	v_pk_add_f32 v[220:221], v[236:237], v[220:221]
	v_pk_add_f32 v[226:227], v[236:237], v[226:227]
	v_pk_add_f32 v[228:229], v[236:237], v[228:229]
	v_rcp_f32_e32 v218, v218
	v_rcp_f32_e32 v219, v219
	v_rcp_f32_e32 v220, v220
	v_rcp_f32_e32 v221, v221
	v_rcp_f32_e32 v226, v226
	v_rcp_f32_e32 v227, v227
	v_rcp_f32_e32 v228, v228
	v_rcp_f32_e32 v229, v229
	v_pk_mul_f32 v[222:223], v[238:239], v[222:223]
	v_pk_mul_f32 v[224:225], v[238:239], v[224:225]
	v_pk_mul_f32 v[230:231], v[238:239], v[230:231]
	v_pk_mul_f32 v[232:233], v[238:239], v[232:233]
	v_pk_mul_f32 v[222:223], v[218:219], v[222:223]
	v_pk_mul_f32 v[224:225], v[220:221], v[224:225]
	v_pk_mul_f32 v[230:231], v[226:227], v[230:231]
	v_pk_mul_f32 v[232:233], v[228:229], v[232:233]
	v_med3_f32 v222, v222, s26, v209
	v_med3_f32 v223, v223, s26, v209
	v_med3_f32 v224, v224, s26, v209
	v_med3_f32 v225, v225, s26, v209
	v_med3_f32 v230, v230, s26, v209
	v_med3_f32 v231, v231, s26, v209
	v_med3_f32 v232, v232, s26, v209
	v_med3_f32 v233, v233, s26, v209
	v_cvt_pk_fp8_f32 v4, v222, v223
	v_cvt_pk_fp8_f32 v4, v224, v225 op_sel:[0,0,1]
	v_cvt_pk_fp8_f32 v5, v230, v231
	v_cvt_pk_fp8_f32 v5, v232, v233 op_sel:[0,0,1]
	s_mov_b32 s12, 0x10000
	v_add_co_u32_e32 v6, vcc, s12, v2
	s_nop 0
	v_addc_co_u32_e32 v7, vcc, 0, v3, vcc
	global_store_dwordx2 v[6:7], v[4:5], off
	v_pk_mul_f32 v[218:219], v[90:91], v[234:235]
	v_pk_mul_f32 v[220:221], v[92:93], v[234:235]
	v_pk_mul_f32 v[226:227], v[78:79], v[234:235]
	v_pk_mul_f32 v[228:229], v[80:81], v[234:235]
	v_exp_f32_e32 v218, v218
	v_exp_f32_e32 v219, v219
	v_exp_f32_e32 v220, v220
	v_exp_f32_e32 v221, v221
	v_exp_f32_e32 v226, v226
	v_exp_f32_e32 v227, v227
	v_exp_f32_e32 v228, v228
	v_exp_f32_e32 v229, v229
	v_pk_mul_f32 v[222:223], v[90:91], v[94:95]
	v_pk_mul_f32 v[224:225], v[92:93], v[96:97]
	v_pk_mul_f32 v[230:231], v[78:79], v[86:87]
	v_pk_mul_f32 v[232:233], v[80:81], v[88:89]
	v_pk_add_f32 v[218:219], v[236:237], v[218:219]
	v_pk_add_f32 v[220:221], v[236:237], v[220:221]
	v_pk_add_f32 v[226:227], v[236:237], v[226:227]
	v_pk_add_f32 v[228:229], v[236:237], v[228:229]
	v_rcp_f32_e32 v218, v218
	v_rcp_f32_e32 v219, v219
	v_rcp_f32_e32 v220, v220
	v_rcp_f32_e32 v221, v221
	v_rcp_f32_e32 v226, v226
	v_rcp_f32_e32 v227, v227
	v_rcp_f32_e32 v228, v228
	v_rcp_f32_e32 v229, v229
	v_pk_mul_f32 v[222:223], v[238:239], v[222:223]
	v_pk_mul_f32 v[224:225], v[238:239], v[224:225]
	v_pk_mul_f32 v[230:231], v[238:239], v[230:231]
	v_pk_mul_f32 v[232:233], v[238:239], v[232:233]
	v_pk_mul_f32 v[222:223], v[218:219], v[222:223]
	v_pk_mul_f32 v[224:225], v[220:221], v[224:225]
	v_pk_mul_f32 v[230:231], v[226:227], v[230:231]
	v_pk_mul_f32 v[232:233], v[228:229], v[232:233]
	v_med3_f32 v222, v222, s26, v209
	v_med3_f32 v223, v223, s26, v209
	v_med3_f32 v224, v224, s26, v209
	v_med3_f32 v225, v225, s26, v209
	v_med3_f32 v230, v230, s26, v209
	v_med3_f32 v231, v231, s26, v209
	v_med3_f32 v232, v232, s26, v209
	v_med3_f32 v233, v233, s26, v209
	v_cvt_pk_fp8_f32 v4, v222, v223
	v_cvt_pk_fp8_f32 v4, v224, v225 op_sel:[0,0,1]
	v_cvt_pk_fp8_f32 v5, v230, v231
	v_cvt_pk_fp8_f32 v5, v232, v233 op_sel:[0,0,1]
	s_mov_b32 s12, 0x18000
	v_add_co_u32_e32 v6, vcc, s12, v2
	s_nop 0
	v_addc_co_u32_e32 v7, vcc, 0, v3, vcc
	global_store_dwordx2 v[6:7], v[4:5], off
	v_pk_mul_f32 v[218:219], v[74:75], v[234:235]
	v_pk_mul_f32 v[220:221], v[76:77], v[234:235]
	v_pk_mul_f32 v[226:227], v[66:67], v[234:235]
	v_pk_mul_f32 v[228:229], v[68:69], v[234:235]
	v_exp_f32_e32 v218, v218
	v_exp_f32_e32 v219, v219
	v_exp_f32_e32 v220, v220
	v_exp_f32_e32 v221, v221
	v_exp_f32_e32 v226, v226
	v_exp_f32_e32 v227, v227
	v_exp_f32_e32 v228, v228
	v_exp_f32_e32 v229, v229
	v_pk_mul_f32 v[222:223], v[74:75], v[82:83]
	v_pk_mul_f32 v[224:225], v[76:77], v[84:85]
	v_pk_mul_f32 v[230:231], v[66:67], v[70:71]
	v_pk_mul_f32 v[232:233], v[68:69], v[72:73]
	v_pk_add_f32 v[218:219], v[236:237], v[218:219]
	v_pk_add_f32 v[220:221], v[236:237], v[220:221]
	v_pk_add_f32 v[226:227], v[236:237], v[226:227]
	v_pk_add_f32 v[228:229], v[236:237], v[228:229]
	v_rcp_f32_e32 v218, v218
	v_rcp_f32_e32 v219, v219
	v_rcp_f32_e32 v220, v220
	v_rcp_f32_e32 v221, v221
	v_rcp_f32_e32 v226, v226
	v_rcp_f32_e32 v227, v227
	v_rcp_f32_e32 v228, v228
	v_rcp_f32_e32 v229, v229
	v_pk_mul_f32 v[222:223], v[238:239], v[222:223]
	v_pk_mul_f32 v[224:225], v[238:239], v[224:225]
	v_pk_mul_f32 v[230:231], v[238:239], v[230:231]
	v_pk_mul_f32 v[232:233], v[238:239], v[232:233]
	v_pk_mul_f32 v[222:223], v[218:219], v[222:223]
	v_pk_mul_f32 v[224:225], v[220:221], v[224:225]
	v_pk_mul_f32 v[230:231], v[226:227], v[230:231]
	v_pk_mul_f32 v[232:233], v[228:229], v[232:233]
	v_med3_f32 v222, v222, s26, v209
	v_med3_f32 v223, v223, s26, v209
	v_med3_f32 v224, v224, s26, v209
	v_med3_f32 v225, v225, s26, v209
	v_med3_f32 v230, v230, s26, v209
	v_med3_f32 v231, v231, s26, v209
	v_med3_f32 v232, v232, s26, v209
	v_med3_f32 v233, v233, s26, v209
	v_cvt_pk_fp8_f32 v4, v222, v223
	v_cvt_pk_fp8_f32 v4, v224, v225 op_sel:[0,0,1]
	v_cvt_pk_fp8_f32 v5, v230, v231
	v_cvt_pk_fp8_f32 v5, v232, v233 op_sel:[0,0,1]
	s_mov_b32 s12, 0x40000
	v_add_co_u32_e32 v6, vcc, s12, v2
	s_nop 0
	v_addc_co_u32_e32 v7, vcc, 0, v3, vcc
	global_store_dwordx2 v[6:7], v[4:5], off
	v_pk_mul_f32 v[218:219], v[58:59], v[234:235]
	v_pk_mul_f32 v[220:221], v[60:61], v[234:235]
	v_pk_mul_f32 v[226:227], v[50:51], v[234:235]
	v_pk_mul_f32 v[228:229], v[52:53], v[234:235]
	v_exp_f32_e32 v218, v218
	v_exp_f32_e32 v219, v219
	v_exp_f32_e32 v220, v220
	v_exp_f32_e32 v221, v221
	v_exp_f32_e32 v226, v226
	v_exp_f32_e32 v227, v227
	v_exp_f32_e32 v228, v228
	v_exp_f32_e32 v229, v229
	v_pk_mul_f32 v[222:223], v[58:59], v[62:63]
	v_pk_mul_f32 v[224:225], v[60:61], v[64:65]
	v_pk_mul_f32 v[230:231], v[50:51], v[54:55]
	v_pk_mul_f32 v[232:233], v[52:53], v[56:57]
	v_pk_add_f32 v[218:219], v[236:237], v[218:219]
	v_pk_add_f32 v[220:221], v[236:237], v[220:221]
	v_pk_add_f32 v[226:227], v[236:237], v[226:227]
	v_pk_add_f32 v[228:229], v[236:237], v[228:229]
	v_rcp_f32_e32 v218, v218
	v_rcp_f32_e32 v219, v219
	v_rcp_f32_e32 v220, v220
	v_rcp_f32_e32 v221, v221
	v_rcp_f32_e32 v226, v226
	v_rcp_f32_e32 v227, v227
	v_rcp_f32_e32 v228, v228
	v_rcp_f32_e32 v229, v229
	v_pk_mul_f32 v[222:223], v[238:239], v[222:223]
	v_pk_mul_f32 v[224:225], v[238:239], v[224:225]
	v_pk_mul_f32 v[230:231], v[238:239], v[230:231]
	v_pk_mul_f32 v[232:233], v[238:239], v[232:233]
	v_pk_mul_f32 v[222:223], v[218:219], v[222:223]
	v_pk_mul_f32 v[224:225], v[220:221], v[224:225]
	v_pk_mul_f32 v[230:231], v[226:227], v[230:231]
	v_pk_mul_f32 v[232:233], v[228:229], v[232:233]
	v_med3_f32 v222, v222, s26, v209
	v_med3_f32 v223, v223, s26, v209
	v_med3_f32 v224, v224, s26, v209
	v_med3_f32 v225, v225, s26, v209
	v_med3_f32 v230, v230, s26, v209
	v_med3_f32 v231, v231, s26, v209
	v_med3_f32 v232, v232, s26, v209
	v_med3_f32 v233, v233, s26, v209
	v_cvt_pk_fp8_f32 v4, v222, v223
	v_cvt_pk_fp8_f32 v4, v224, v225 op_sel:[0,0,1]
	v_cvt_pk_fp8_f32 v5, v230, v231
	v_cvt_pk_fp8_f32 v5, v232, v233 op_sel:[0,0,1]
	s_mov_b32 s12, 0x48000
	v_add_co_u32_e32 v6, vcc, s12, v2
	s_nop 0
	v_addc_co_u32_e32 v7, vcc, 0, v3, vcc
	global_store_dwordx2 v[6:7], v[4:5], off
	v_pk_mul_f32 v[218:219], v[42:43], v[234:235]
	v_pk_mul_f32 v[220:221], v[44:45], v[234:235]
	v_pk_mul_f32 v[226:227], v[34:35], v[234:235]
	v_pk_mul_f32 v[228:229], v[36:37], v[234:235]
	v_exp_f32_e32 v218, v218
	v_exp_f32_e32 v219, v219
	v_exp_f32_e32 v220, v220
	v_exp_f32_e32 v221, v221
	v_exp_f32_e32 v226, v226
	v_exp_f32_e32 v227, v227
	v_exp_f32_e32 v228, v228
	v_exp_f32_e32 v229, v229
	v_pk_mul_f32 v[222:223], v[42:43], v[46:47]
	v_pk_mul_f32 v[224:225], v[44:45], v[48:49]
	v_pk_mul_f32 v[230:231], v[34:35], v[38:39]
	v_pk_mul_f32 v[232:233], v[36:37], v[40:41]
	v_pk_add_f32 v[218:219], v[236:237], v[218:219]
	v_pk_add_f32 v[220:221], v[236:237], v[220:221]
	v_pk_add_f32 v[226:227], v[236:237], v[226:227]
	v_pk_add_f32 v[228:229], v[236:237], v[228:229]
	v_rcp_f32_e32 v218, v218
	v_rcp_f32_e32 v219, v219
	v_rcp_f32_e32 v220, v220
	v_rcp_f32_e32 v221, v221
	v_rcp_f32_e32 v226, v226
	v_rcp_f32_e32 v227, v227
	v_rcp_f32_e32 v228, v228
	v_rcp_f32_e32 v229, v229
	v_pk_mul_f32 v[222:223], v[238:239], v[222:223]
	v_pk_mul_f32 v[224:225], v[238:239], v[224:225]
	v_pk_mul_f32 v[230:231], v[238:239], v[230:231]
	v_pk_mul_f32 v[232:233], v[238:239], v[232:233]
	v_pk_mul_f32 v[222:223], v[218:219], v[222:223]
	v_pk_mul_f32 v[224:225], v[220:221], v[224:225]
	v_pk_mul_f32 v[230:231], v[226:227], v[230:231]
	v_pk_mul_f32 v[232:233], v[228:229], v[232:233]
	v_med3_f32 v222, v222, s26, v209
	v_med3_f32 v223, v223, s26, v209
	v_med3_f32 v224, v224, s26, v209
	v_med3_f32 v225, v225, s26, v209
	v_med3_f32 v230, v230, s26, v209
	v_med3_f32 v231, v231, s26, v209
	v_med3_f32 v232, v232, s26, v209
	v_med3_f32 v233, v233, s26, v209
	v_cvt_pk_fp8_f32 v4, v222, v223
	v_cvt_pk_fp8_f32 v4, v224, v225 op_sel:[0,0,1]
	v_cvt_pk_fp8_f32 v5, v230, v231
	v_cvt_pk_fp8_f32 v5, v232, v233 op_sel:[0,0,1]
	s_mov_b32 s12, 0x50000
	v_add_co_u32_e32 v6, vcc, s12, v2
	s_nop 0
	v_addc_co_u32_e32 v7, vcc, 0, v3, vcc
	global_store_dwordx2 v[6:7], v[4:5], off
	v_pk_mul_f32 v[218:219], v[26:27], v[234:235]
	v_pk_mul_f32 v[220:221], v[28:29], v[234:235]
	v_pk_mul_f32 v[226:227], v[18:19], v[234:235]
	v_pk_mul_f32 v[228:229], v[20:21], v[234:235]
	v_exp_f32_e32 v218, v218
	v_exp_f32_e32 v219, v219
	v_exp_f32_e32 v220, v220
	v_exp_f32_e32 v221, v221
	v_exp_f32_e32 v226, v226
	v_exp_f32_e32 v227, v227
	v_exp_f32_e32 v228, v228
	v_exp_f32_e32 v229, v229
	v_pk_mul_f32 v[222:223], v[26:27], v[30:31]
	v_pk_mul_f32 v[224:225], v[28:29], v[32:33]
	v_pk_mul_f32 v[230:231], v[18:19], v[22:23]
	v_pk_mul_f32 v[232:233], v[20:21], v[24:25]
	v_pk_add_f32 v[218:219], v[236:237], v[218:219]
	v_pk_add_f32 v[220:221], v[236:237], v[220:221]
	v_pk_add_f32 v[226:227], v[236:237], v[226:227]
	v_pk_add_f32 v[228:229], v[236:237], v[228:229]
	v_rcp_f32_e32 v218, v218
	v_rcp_f32_e32 v219, v219
	v_rcp_f32_e32 v220, v220
	v_rcp_f32_e32 v221, v221
	v_rcp_f32_e32 v226, v226
	v_rcp_f32_e32 v227, v227
	v_rcp_f32_e32 v228, v228
	v_rcp_f32_e32 v229, v229
	v_pk_mul_f32 v[222:223], v[238:239], v[222:223]
	v_pk_mul_f32 v[224:225], v[238:239], v[224:225]
	v_pk_mul_f32 v[230:231], v[238:239], v[230:231]
	v_pk_mul_f32 v[232:233], v[238:239], v[232:233]
	v_pk_mul_f32 v[222:223], v[218:219], v[222:223]
	v_pk_mul_f32 v[224:225], v[220:221], v[224:225]
	v_pk_mul_f32 v[230:231], v[226:227], v[230:231]
	v_pk_mul_f32 v[232:233], v[228:229], v[232:233]
	v_med3_f32 v222, v222, s26, v209
	v_med3_f32 v223, v223, s26, v209
	v_med3_f32 v224, v224, s26, v209
	v_med3_f32 v225, v225, s26, v209
	v_med3_f32 v230, v230, s26, v209
	v_med3_f32 v231, v231, s26, v209
	v_med3_f32 v232, v232, s26, v209
	v_med3_f32 v233, v233, s26, v209
	v_cvt_pk_fp8_f32 v4, v222, v223
	v_cvt_pk_fp8_f32 v4, v224, v225 op_sel:[0,0,1]
	v_cvt_pk_fp8_f32 v5, v230, v231
	v_cvt_pk_fp8_f32 v5, v232, v233 op_sel:[0,0,1]
	v_add_co_u32_e32 v2, vcc, 0x58000, v2
	s_nop 0
	v_addc_co_u32_e32 v3, vcc, 0, v3, vcc
	s_and_b64 vcc, exec, s[4:5]
	s_mov_b32 s12, s6
	s_mov_b32 s59, s7
	s_mov_b64 s[60:61], s[8:9]
	s_mov_b64 s[18:19], s[10:11]
	global_store_dwordx2 v[2:3], v[4:5], off
	s_cbranch_vccz .LBB0_1416
	s_waitcnt vmcnt(0)
	s_setprio 0
	s_cmpk_gt_u32 s27, 0xff
	s_movk_i32 s47, 0x900
	s_cbranch_scc1 .LBB0_1423
	s_barrier
